# speedup vs baseline: 1.0315x; 1.0167x over previous
.LBB3_2:
	v_lshrrev_b32_e32 v87, 1, v0
	v_add_u32_e32 v64, s6, v87
	v_and_b32_e32 v61, 1, v0
	s_add_i32 s7, s14, 0x187
	v_cmp_gt_i32_e64 s[6:7], s7, v64
	v_mov_b32_e32 v85, 0
	v_ashrrev_i32_e32 v65, 31, v64
	v_mov_b32_e32 v66, 0
	v_mov_b32_e32 v67, 0
	s_and_saveexec_b64 s[10:11], s[6:7]
	s_cbranch_execz .LBB3_6
	s_load_dwordx2 s[14:15], s[0:1], 0x10
	v_lshlrev_b32_e32 v59, 2, v87
	global_load_dwordx2 v[66:67], v59, s[12:13]
	v_mov_b32_e32 v85, 0
	v_cmp_eq_u32_e32 vcc, 0, v61
	s_waitcnt lgkmcnt(0)
	v_lshl_add_u64 v[88:89], v[64:65], 2, s[14:15]
	global_load_dword v59, v[88:89], off
	s_and_saveexec_b64 s[12:13], vcc
	s_cbranch_execz .LBB3_5
	v_lshl_add_u64 v[88:89], v[64:65], 2, s[4:5]
	global_load_dword v85, v[88:89], off

.LBB3_14:
	v_mov_b32_e32 v1, 0x1e6a0
	v_lshl_add_u32 v1, v0, 2, v1
	s_waitcnt vmcnt(7)
	ds_write_b32 v1, v77
.LBB3_15:
	s_or_b64 exec, exec, s[0:1]
	v_or_b32_e32 v1, 0x1c00, v0
	v_cmp_gt_u32_e32 vcc, s17, v1
	s_and_saveexec_b64 s[0:1], vcc
	s_cbranch_execz .LBB3_17
	v_mov_b32_e32 v1, 0x1f6a0
	v_lshl_add_u32 v1, v0, 2, v1
	s_waitcnt vmcnt(6)
	ds_write_b32 v1, v75
.LBB3_17:
	s_or_b64 exec, exec, s[0:1]
	v_or_b32_e32 v1, 0x2000, v0
	v_cmp_gt_u32_e32 vcc, s17, v1
	s_and_saveexec_b64 s[0:1], vcc
	s_cbranch_execz .LBB3_19
	v_mov_b32_e32 v1, 0x206a0
	v_lshl_add_u32 v1, v0, 2, v1
	s_waitcnt vmcnt(5)
	ds_write_b32 v1, v80
.LBB3_19:
	s_or_b64 exec, exec, s[0:1]
	v_or_b32_e32 v1, 0x2400, v0
	v_cmp_gt_u32_e32 vcc, s17, v1
	s_and_saveexec_b64 s[0:1], vcc
	s_cbranch_execz .LBB3_21
	v_mov_b32_e32 v1, 0x216a0
	v_lshl_add_u32 v1, v0, 2, v1
	s_waitcnt vmcnt(4)
	ds_write_b32 v1, v78
.LBB3_21:
	s_or_b64 exec, exec, s[0:1]
	v_or_b32_e32 v1, 0x2800, v0
	v_cmp_gt_u32_e32 vcc, s17, v1
	s_and_saveexec_b64 s[0:1], vcc
	s_cbranch_execz .LBB3_23
	v_mov_b32_e32 v1, 0x226a0
	v_lshl_add_u32 v1, v0, 2, v1
	s_waitcnt vmcnt(3)
	ds_write_b32 v1, v76
.LBB3_23:
	s_or_b64 exec, exec, s[0:1]
	v_or_b32_e32 v1, 0x2c00, v0
	v_cmp_gt_u32_e32 vcc, s17, v1
	s_and_saveexec_b64 s[0:1], vcc
	s_cbranch_execz .LBB3_25
	v_mov_b32_e32 v1, 0x236a0
	v_lshl_add_u32 v1, v0, 2, v1
	s_waitcnt vmcnt(2)
	ds_write_b32 v1, v74
.LBB3_25:
	s_or_b64 exec, exec, s[0:1]
	v_or_b32_e32 v1, 0x3000, v0
	v_cmp_gt_u32_e32 vcc, s17, v1
	s_and_saveexec_b64 s[0:1], vcc
	s_cbranch_execz .LBB3_27
	v_mov_b32_e32 v1, 0x246a0
	v_lshl_add_u32 v1, v0, 2, v1
	s_waitcnt vmcnt(1)
	ds_write_b32 v1, v73
.LBB3_27:
	s_or_b64 exec, exec, s[0:1]
	v_or_b32_e32 v1, 0x3400, v0
	v_cmp_gt_u32_e32 vcc, s17, v1
	s_and_saveexec_b64 s[0:1], vcc
	s_cbranch_execz .LBB3_29
	v_mov_b32_e32 v1, 0x256a0
	v_lshl_add_u32 v0, v0, 2, v1
	s_waitcnt vmcnt(0)
	ds_write_b32 v0, v63

.LBB3_30:
	s_waitcnt vmcnt(0)
	s_waitcnt lgkmcnt(0)
	s_load_dwordx2 s[32:33], s[12:13], 0x80
	v_subrev_u32_e32 v63, s16, v61
	s_cmpk_gt_i32 s17, 0x3800
	s_waitcnt vmcnt(1)
	v_add_u32_e32 v63, v63, v66
	v_add_u32_e32 v68, v66, v61
	v_subrev_u32_e32 v66, s16, v67
	s_mov_b64 s[16:17], 0x34d40
	v_lshl_add_u64 v[72:73], v[94:95], 0, s[16:17]
	s_mov_b64 s[16:17], 0x38d40
	v_lshl_add_u64 v[74:75], v[94:95], 0, s[16:17]
	s_mov_b64 s[16:17], 0x3cd40
	v_lshl_add_u64 v[76:77], v[94:95], 0, s[16:17]
	s_mov_b64 s[16:17], 0x40d40
	v_lshl_add_u64 v[78:79], v[94:95], 0, s[16:17]
	s_mov_b64 s[16:17], 0x44d40
	v_lshl_add_u64 v[80:81], v[94:95], 0, s[16:17]
	s_mov_b64 s[16:17], 0x1c6a0
	v_lshl_add_u64 v[86:87], v[94:95], 0, s[16:17]
	s_mov_b64 s[16:17], 0x206a0
	s_waitcnt vmcnt(0)
	v_cvt_f32_f16_sdwa v1, v85 dst_sel:DWORD dst_unused:UNUSED_PAD src0_sel:WORD_1
	v_cvt_f32_f16_e32 v0, v85
	s_movk_i32 s0, 0x186a
	v_lshl_add_u64 v[88:89], v[94:95], 0, s[16:17]
	s_mov_b64 s[16:17], 0x246a0
	v_cmp_gt_u32_e64 s[4:5], s0, v69
	s_mov_b64 s[0:1], 0x30d40
	v_lshl_add_u64 v[90:91], v[94:95], 0, s[16:17]
	s_mov_b64 s[16:17], 0x286a0
	v_lshlrev_b32_e32 v104, 4, v69
	v_lshl_add_u64 v[70:71], v[94:95], 0, s[0:1]
	v_lshl_add_u64 v[82:83], v[96:97], 0, s[0:1]
	s_mov_b64 s[0:1], 0x186a0
	v_lshl_add_u64 v[92:93], v[94:95], 0, s[16:17]
	s_mov_b64 s[16:17], 0x2c6a0
	v_ashrrev_i32_e32 v69, 31, v68
	s_cselect_b64 s[10:11], -1, 0
	v_cmp_lt_i32_e64 s[2:3], v68, v67
	v_lshl_add_u64 v[84:85], v[94:95], 0, s[0:1]
	v_lshl_add_u64 v[94:95], v[94:95], 0, s[16:17]
	v_lshl_add_u64 v[96:97], v[96:97], 0, s[0:1]
	v_lshl_add_u64 v[98:99], v[68:69], 2, s[8:9]
	s_mov_b32 s20, 0
	s_mov_b64 s[8:9], -1
	s_movk_i32 s22, 0x61a8
	v_mov_b32_e32 v69, 0x186a0
	v_mov_b32_e32 v105, 0x186a8
	v_mov_b32_e32 v106, 0x186b0
	v_mov_b32_e32 v107, 0x186b8
	v_mov_b32_e32 v114, 0x266c0
	v_mov_b32_e32 v113, 0
	ds_write_b32 v114, v113
	s_branch .LBB3_32
.LBB3_31:
	s_cmp_lg_u64 s[0:1], 0
	s_cbranch_scc1 .Lk4_nopfA2
	s_cmp_eq_u32 s34, 0
	s_cbranch_scc1 .Lk4_nopfA2
	global_load_dwordx4 v[2:5], v[70:71], off
	global_load_dwordx4 v[6:9], v[72:73], off
	global_load_dwordx4 v[10:13], v[74:75], off
	global_load_dwordx4 v[14:17], v[76:77], off
	global_load_dwordx4 v[18:21], v[78:79], off
	global_load_dwordx4 v[22:25], v[80:81], off
	global_load_dwordx4 v[26:29], v[82:83], off
.Lk4_nopfA2:
	s_mov_b64 s[36:37], 0x30d40
	v_lshl_add_u64 v[84:85], v[84:85], 0, s[36:37]
	v_lshl_add_u64 v[86:87], v[86:87], 0, s[36:37]
	v_lshl_add_u64 v[88:89], v[88:89], 0, s[36:37]
	v_lshl_add_u64 v[90:91], v[90:91], 0, s[36:37]
	v_lshl_add_u64 v[92:93], v[92:93], 0, s[36:37]
	v_lshl_add_u64 v[94:95], v[94:95], 0, s[36:37]
	v_lshl_add_u64 v[96:97], v[96:97], 0, s[36:37]
	s_mov_b32 s20, 0xc350
	s_mov_b64 s[8:9], 0
	s_and_b64 vcc, exec, s[16:17]
	s_barrier
	s_cbranch_vccnz .LBB3_81

.LBB3_34:
	s_or_b64 exec, exec, s[0:1]
	s_mov_b64 s[0:1], -1
	s_and_b64 vcc, exec, s[10:11]
	s_waitcnt lgkmcnt(0)
	s_barrier
	s_cmp_lg_u32 s34, 0
	s_cbranch_scc1 .Lk4_nopfB1
	global_load_dwordx4 v[30:33], v[84:85], off
	global_load_dwordx4 v[34:37], v[86:87], off
	global_load_dwordx4 v[38:41], v[88:89], off
	global_load_dwordx4 v[42:45], v[90:91], off
	global_load_dwordx4 v[46:49], v[92:93], off
	global_load_dwordx4 v[50:53], v[94:95], off
	global_load_dwordx4 v[54:57], v[96:97], off

.LBB3_45:
	v_sub_u32_e32 v113, v66, v63
	v_lshl_add_u32 v108, v63, 2, v69
	v_cmp_lt_i32_e32 vcc, 0, v113
	v_cmp_lt_i32_e64 s[24:25], 2, v113
	v_cmp_lt_i32_e64 s[26:27], 4, v113
	v_cmp_lt_i32_e64 s[28:29], 6, v113
	v_cndmask_b32_e32 v108, v69, v108, vcc
	ds_read2_b32 v[100:101], v108 offset1:2
	ds_read2_b32 v[102:103], v108 offset0:4 offset1:6
	s_waitcnt lgkmcnt(0)
	v_subrev_u32_e32 v100, s20, v100
	v_subrev_u32_e32 v101, s20, v101
	v_subrev_u32_e32 v102, s20, v102
	v_subrev_u32_e32 v103, s20, v103
	v_cmp_gt_u32_e64 s[30:31], s22, v100
	v_cmp_gt_u32_e64 s[38:39], s22, v101
	v_cmp_gt_u32_e64 s[40:41], s22, v102
	v_cmp_gt_u32_e64 s[42:43], s22, v103
	v_lshlrev_b32_e32 v100, 2, v100
	v_lshlrev_b32_e32 v101, 2, v101
	v_lshlrev_b32_e32 v102, 2, v102
	v_lshlrev_b32_e32 v103, 2, v103
	s_and_b64 vcc, vcc, s[30:31]
	s_and_b64 s[24:25], s[24:25], s[38:39]
	s_and_b64 s[26:27], s[26:27], s[40:41]
	s_and_b64 s[28:29], s[28:29], s[42:43]
	v_cndmask_b32_e32 v100, v114, v100, vcc
	v_cndmask_b32_e64 v101, v114, v101, s[24:25]
	v_cndmask_b32_e64 v102, v114, v102, s[26:27]
	v_cndmask_b32_e64 v103, v114, v103, s[28:29]
	ds_read_b32 v108, v100
	ds_read_b32 v109, v101
	ds_read_b32 v110, v102
	ds_read_b32 v111, v103
	v_cndmask_b32_e64 v112, 0, 1, vcc
	v_addc_co_u32_e64 v112, s[30:31], 0, v112, s[24:25]
	v_addc_co_u32_e64 v112, s[30:31], 0, v112, s[26:27]
	v_addc_co_u32_e64 v112, s[30:31], 0, v112, s[28:29]
	v_cmp_gt_u32_e32 vcc, 4, v112
	v_lshl_add_u32 v63, v112, 1, v63
	s_or_b64 s[16:17], vcc, s[16:17]
	s_waitcnt lgkmcnt(0)
	v_fma_mix_f32 v0, v108, 1.0, v0 op_sel_hi:[1,0,0]
	v_fma_mix_f32 v1, v108, 1.0, v1 op_sel:[1,0,0] op_sel_hi:[1,0,0]
	v_fma_mix_f32 v0, v109, 1.0, v0 op_sel_hi:[1,0,0]
	v_fma_mix_f32 v1, v109, 1.0, v1 op_sel:[1,0,0] op_sel_hi:[1,0,0]
	v_fma_mix_f32 v0, v110, 1.0, v0 op_sel_hi:[1,0,0]
	v_fma_mix_f32 v1, v110, 1.0, v1 op_sel:[1,0,0] op_sel_hi:[1,0,0]
	v_fma_mix_f32 v0, v111, 1.0, v0 op_sel_hi:[1,0,0]
	v_fma_mix_f32 v1, v111, 1.0, v1 op_sel:[1,0,0] op_sel_hi:[1,0,0]
	s_andn2_b64 exec, exec, s[16:17]
	s_cbranch_execnz .LBB3_45
	s_branch .LBB3_54

.LBB3_55:
	v_cndmask_b32_e64 v100, 0, 1, s[8:9]
	s_xor_b64 s[16:17], s[8:9], -1
	v_cmp_ne_u32_e64 s[0:1], 1, v100
	s_cmp_eq_u32 s34, 0
	s_cbranch_scc1 .Lk4_nopfB2
	global_load_dwordx4 v[30:33], v[84:85], off
	global_load_dwordx4 v[34:37], v[86:87], off
	global_load_dwordx4 v[38:41], v[88:89], off
	global_load_dwordx4 v[42:45], v[90:91], off
	global_load_dwordx4 v[46:49], v[92:93], off
	global_load_dwordx4 v[50:53], v[94:95], off
	global_load_dwordx4 v[54:57], v[96:97], off
.Lk4_nopfB2:
.LBB3_57:
	s_barrier
	s_waitcnt vmcnt(6)
	ds_write_b128 v58, v[30:33]
	s_waitcnt vmcnt(5)
	ds_write_b128 v58, v[34:37] offset:16384
	s_waitcnt vmcnt(4)
	ds_write_b128 v58, v[38:41] offset:32768
	s_waitcnt vmcnt(3)
	ds_write_b128 v58, v[42:45] offset:49152
	s_waitcnt vmcnt(2)
	ds_write_b128 v60, v[46:49]
	s_waitcnt vmcnt(1)
	ds_write_b128 v62, v[50:53]
	s_and_saveexec_b64 s[8:9], s[4:5]
	s_cbranch_execz .LBB3_59
	s_waitcnt vmcnt(0)
	ds_write_b128 v104, v[54:57]
.LBB3_59:
	s_or_b64 exec, exec, s[8:9]
	s_add_i32 s23, s20, 0x61a8
	s_mov_b64 s[8:9], -1
	s_and_b64 vcc, exec, s[10:11]
	s_waitcnt lgkmcnt(0)
	s_barrier
	s_cmp_lg_u32 s20, 0
	s_cbranch_scc1 .Lk4_nopfA1
	s_cmp_lg_u32 s34, 0
	s_cbranch_scc1 .Lk4_nopfA1
	global_load_dwordx4 v[2:5], v[70:71], off
	global_load_dwordx4 v[6:9], v[72:73], off
	global_load_dwordx4 v[10:13], v[74:75], off
	global_load_dwordx4 v[14:17], v[76:77], off
	global_load_dwordx4 v[18:21], v[78:79], off
	global_load_dwordx4 v[22:25], v[80:81], off
	global_load_dwordx4 v[26:29], v[82:83], off

.LBB3_70:
	v_sub_u32_e32 v113, v66, v63
	v_lshl_add_u32 v108, v63, 2, v69
	v_cmp_lt_i32_e32 vcc, 0, v113
	v_cmp_lt_i32_e64 s[24:25], 2, v113
	v_cmp_lt_i32_e64 s[26:27], 4, v113
	v_cmp_lt_i32_e64 s[28:29], 6, v113
	v_cndmask_b32_e32 v108, v69, v108, vcc
	ds_read2_b32 v[100:101], v108 offset1:2
	ds_read2_b32 v[102:103], v108 offset0:4 offset1:6
	s_waitcnt lgkmcnt(0)
	v_subrev_u32_e32 v100, s23, v100
	v_subrev_u32_e32 v101, s23, v101
	v_subrev_u32_e32 v102, s23, v102
	v_subrev_u32_e32 v103, s23, v103
	v_cmp_gt_u32_e64 s[30:31], s22, v100
	v_cmp_gt_u32_e64 s[38:39], s22, v101
	v_cmp_gt_u32_e64 s[40:41], s22, v102
	v_cmp_gt_u32_e64 s[42:43], s22, v103
	v_lshlrev_b32_e32 v100, 2, v100
	v_lshlrev_b32_e32 v101, 2, v101
	v_lshlrev_b32_e32 v102, 2, v102
	v_lshlrev_b32_e32 v103, 2, v103
	s_and_b64 vcc, vcc, s[30:31]
	s_and_b64 s[24:25], s[24:25], s[38:39]
	s_and_b64 s[26:27], s[26:27], s[40:41]
	s_and_b64 s[28:29], s[28:29], s[42:43]
	v_cndmask_b32_e32 v100, v114, v100, vcc
	v_cndmask_b32_e64 v101, v114, v101, s[24:25]
	v_cndmask_b32_e64 v102, v114, v102, s[26:27]
	v_cndmask_b32_e64 v103, v114, v103, s[28:29]
	ds_read_b32 v108, v100
	ds_read_b32 v109, v101
	ds_read_b32 v110, v102
	ds_read_b32 v111, v103
	v_cndmask_b32_e64 v112, 0, 1, vcc
	v_addc_co_u32_e64 v112, s[30:31], 0, v112, s[24:25]
	v_addc_co_u32_e64 v112, s[30:31], 0, v112, s[26:27]
	v_addc_co_u32_e64 v112, s[30:31], 0, v112, s[28:29]
	v_cmp_gt_u32_e32 vcc, 4, v112
	v_lshl_add_u32 v63, v112, 1, v63
	s_or_b64 s[18:19], vcc, s[18:19]
	s_waitcnt lgkmcnt(0)
	v_fma_mix_f32 v0, v108, 1.0, v0 op_sel_hi:[1,0,0]
	v_fma_mix_f32 v1, v108, 1.0, v1 op_sel:[1,0,0] op_sel_hi:[1,0,0]
	v_fma_mix_f32 v0, v109, 1.0, v0 op_sel_hi:[1,0,0]
	v_fma_mix_f32 v1, v109, 1.0, v1 op_sel:[1,0,0] op_sel_hi:[1,0,0]
	v_fma_mix_f32 v0, v110, 1.0, v0 op_sel_hi:[1,0,0]
	v_fma_mix_f32 v1, v110, 1.0, v1 op_sel:[1,0,0] op_sel_hi:[1,0,0]
	v_fma_mix_f32 v0, v111, 1.0, v0 op_sel_hi:[1,0,0]
	v_fma_mix_f32 v1, v111, 1.0, v1 op_sel:[1,0,0] op_sel_hi:[1,0,0]
	s_andn2_b64 exec, exec, s[18:19]
	s_cbranch_execnz .LBB3_70
	s_branch .LBB3_79

.LBB3_84:
	v_mov_b32_e32 v87, 0x186a0
	v_lshl_add_u32 v87, v0, 2, v87
	s_waitcnt vmcnt(13)
	ds_write_b32 v87, v86
	s_or_b64 exec, exec, s[0:1]
	v_cmp_gt_u32_e32 vcc, s17, v72
	s_and_saveexec_b64 s[0:1], vcc
	s_cbranch_execz .LBB3_9
.LBB3_85:
	v_mov_b32_e32 v72, 0x196a0
	v_lshl_add_u32 v72, v0, 2, v72
	s_waitcnt vmcnt(12)
	ds_write_b32 v72, v84
	s_or_b64 exec, exec, s[0:1]
	v_cmp_gt_u32_e32 vcc, s17, v71
	s_and_saveexec_b64 s[0:1], vcc
	s_cbranch_execz .LBB3_10
.LBB3_86:
	v_mov_b32_e32 v71, 0x1a6a0
	v_lshl_add_u32 v71, v0, 2, v71
	s_waitcnt vmcnt(11)
	ds_write_b32 v71, v83
	s_or_b64 exec, exec, s[0:1]
	v_cmp_gt_u32_e32 vcc, s17, v70
	s_and_saveexec_b64 s[0:1], vcc
	s_cbranch_execz .LBB3_11
.LBB3_87:
	v_mov_b32_e32 v70, 0x1b6a0
	v_lshl_add_u32 v70, v0, 2, v70
	s_waitcnt vmcnt(10)
	ds_write_b32 v70, v82
	s_or_b64 exec, exec, s[0:1]
	v_cmp_gt_u32_e32 vcc, s17, v68
	s_and_saveexec_b64 s[0:1], vcc
	s_cbranch_execz .LBB3_12
.LBB3_88:
	v_mov_b32_e32 v68, 0x1c6a0
	v_lshl_add_u32 v68, v0, 2, v68
	s_waitcnt vmcnt(9)
	ds_write_b32 v68, v81
	s_or_b64 exec, exec, s[0:1]
	v_cmp_gt_u32_e32 vcc, s17, v1
	s_and_saveexec_b64 s[0:1], vcc
	s_cbranch_execz .LBB3_13
.LBB3_89:
	v_mov_b32_e32 v1, 0x1d6a0
	v_lshl_add_u32 v1, v0, 2, v1
	s_waitcnt vmcnt(8)
	ds_write_b32 v1, v79
	s_or_b64 exec, exec, s[0:1]
	v_cmp_gt_u32_e32 vcc, s17, v69
	s_and_saveexec_b64 s[0:1], vcc
	s_cbranch_execnz .LBB3_14
	s_branch .LBB3_15

	.amdhsa_kernel _Z8k_layer2PKiS0_PKfPKjS2_P15HIP_vector_typeIfLj2EE
		.amdhsa_group_segment_fixed_size 157408
		.amdhsa_private_segment_fixed_size 0
		.amdhsa_kernarg_size 48
		.amdhsa_user_sgpr_count 2
		.amdhsa_user_sgpr_dispatch_ptr 0
		.amdhsa_user_sgpr_queue_ptr 0
		.amdhsa_user_sgpr_kernarg_segment_ptr 1
		.amdhsa_user_sgpr_dispatch_id 0
		.amdhsa_user_sgpr_kernarg_preload_length 0
		.amdhsa_user_sgpr_kernarg_preload_offset 0
		.amdhsa_user_sgpr_private_segment_size 0
		.amdhsa_uses_dynamic_stack 0
		.amdhsa_enable_private_segment 0
		.amdhsa_system_sgpr_workgroup_id_x 1
		.amdhsa_system_sgpr_workgroup_id_y 0
		.amdhsa_system_sgpr_workgroup_id_z 0
		.amdhsa_system_sgpr_workgroup_info 0
		.amdhsa_system_vgpr_workitem_id 0
		.amdhsa_next_free_vgpr 115
		.amdhsa_next_free_sgpr 96
		.amdhsa_accum_offset 116
		.amdhsa_reserve_vcc 1
		.amdhsa_float_round_mode_32 0
		.amdhsa_float_round_mode_16_64 0
		.amdhsa_float_denorm_mode_32 3
		.amdhsa_float_denorm_mode_16_64 3
		.amdhsa_dx10_clamp 1
		.amdhsa_ieee_mode 1
		.amdhsa_fp16_overflow 0
		.amdhsa_tg_split 0
		.amdhsa_exception_fp_ieee_invalid_op 0
		.amdhsa_exception_fp_denorm_src 0
		.amdhsa_exception_fp_ieee_div_zero 0
		.amdhsa_exception_fp_ieee_overflow 0
		.amdhsa_exception_fp_ieee_underflow 0
		.amdhsa_exception_fp_ieee_inexact 0
		.amdhsa_exception_int_div_zero 0
	.end_amdhsa_kernel

amdhsa.kernels:
  - .agpr_count:     0
    .args:
      - .actual_access:  read_only
        .address_space:  global
        .offset:         0
        .size:           8
        .value_kind:     global_buffer
      - .actual_access:  read_only
        .address_space:  global
        .offset:         8
        .size:           8
        .value_kind:     global_buffer
      - .actual_access:  write_only
        .address_space:  global
        .offset:         16
        .size:           8
        .value_kind:     global_buffer
      - .actual_access:  write_only
        .address_space:  global
        .offset:         24
        .size:           8
        .value_kind:     global_buffer
      - .actual_access:  read_only
        .address_space:  global
        .offset:         32
        .size:           8
        .value_kind:     global_buffer
      - .actual_access:  read_only
        .address_space:  global
        .offset:         40
        .size:           8
        .value_kind:     global_buffer
      - .actual_access:  read_only
        .address_space:  global
        .offset:         48
        .size:           8
        .value_kind:     global_buffer
      - .actual_access:  read_only
        .address_space:  global
        .offset:         56
        .size:           8
        .value_kind:     global_buffer
      - .actual_access:  write_only
        .address_space:  global
        .offset:         64
        .size:           8
        .value_kind:     global_buffer
      - .actual_access:  read_only
        .address_space:  global
        .offset:         72
        .size:           8
        .value_kind:     global_buffer
      - .actual_access:  write_only
        .address_space:  global
        .offset:         80
        .size:           8
        .value_kind:     global_buffer
    .group_segment_fixed_size: 55632
    .kernarg_segment_align: 8
    .kernarg_segment_size: 88
    .language:       OpenCL C
    .language_version:
      - 2
      - 0
    .max_flat_workgroup_size: 1024
    .name:           _Z9k_scatterPKiS0_PiPjPKfS4_S4_S4_PfS4_PDv4_j
    .private_segment_fixed_size: 0
    .sgpr_count:     58
    .sgpr_spill_count: 0
    .symbol:         _Z9k_scatterPKiS0_PiPjPKfS4_S4_S4_PfS4_PDv4_j.kd
    .uniform_work_group_size: 1
    .uses_dynamic_stack: false
    .vgpr_count:     114
    .vgpr_spill_count: 0
    .wavefront_size: 64
  - .agpr_count:     0
    .args:
      - .actual_access:  read_only
        .address_space:  global
        .offset:         0
        .size:           8
        .value_kind:     global_buffer
      - .actual_access:  read_only
        .address_space:  global
        .offset:         8
        .size:           8
        .value_kind:     global_buffer
      - .actual_access:  read_only
        .address_space:  global
        .offset:         16
        .size:           8
        .value_kind:     global_buffer
      - .actual_access:  read_only
        .address_space:  global
        .offset:         24
        .size:           8
        .value_kind:     global_buffer
      - .actual_access:  write_only
        .address_space:  global
        .offset:         32
        .size:           8
        .value_kind:     global_buffer
      - .actual_access:  write_only
        .address_space:  global
        .offset:         40
        .size:           8
        .value_kind:     global_buffer
      - .actual_access:  write_only
        .address_space:  global
        .offset:         48
        .size:           8
        .value_kind:     global_buffer
      - .actual_access:  write_only
        .address_space:  global
        .offset:         56
        .size:           8
        .value_kind:     global_buffer
    .group_segment_fixed_size: 37232
    .kernarg_segment_align: 8
    .kernarg_segment_size: 64
    .language:       OpenCL C
    .language_version:
      - 2
      - 0
    .max_flat_workgroup_size: 256
    .name:           _Z9k_binsortPKjPKiPKfPKDv4_jPiS8_PfP6__half
    .private_segment_fixed_size: 0
    .sgpr_count:     104
    .sgpr_spill_count: 0
    .symbol:         _Z9k_binsortPKjPKiPKfPKDv4_jPiS8_PfP6__half.kd
    .uniform_work_group_size: 1
    .uses_dynamic_stack: false
    .vgpr_count:     168
    .vgpr_spill_count: 0
    .wavefront_size: 64
  - .agpr_count:     0
    .args:
      - .actual_access:  read_only
        .address_space:  global
        .offset:         0
        .size:           8
        .value_kind:     global_buffer
      - .actual_access:  read_only
        .address_space:  global
        .offset:         8
        .size:           8
        .value_kind:     global_buffer
      - .actual_access:  read_only
        .address_space:  global
        .offset:         16
        .size:           8
        .value_kind:     global_buffer
      - .actual_access:  read_only
        .address_space:  global
        .offset:         24
        .size:           8
        .value_kind:     global_buffer
      - .actual_access:  read_only
        .address_space:  global
        .offset:         32
        .size:           8
        .value_kind:     global_buffer
      - .actual_access:  read_only
        .address_space:  global
        .offset:         40
        .size:           8
        .value_kind:     global_buffer
      - .actual_access:  write_only
        .address_space:  global
        .offset:         48
        .size:           8
        .value_kind:     global_buffer
    .group_segment_fixed_size: 6272
    .kernarg_segment_align: 8
    .kernarg_segment_size: 56
    .language:       OpenCL C
    .language_version:
      - 2
      - 0
    .max_flat_workgroup_size: 64
    .name:           _Z8k_layer1PKiS0_PKfPK6__halfS2_S2_P7__half2
    .private_segment_fixed_size: 0
    .sgpr_count:     22
    .sgpr_spill_count: 0
    .symbol:         _Z8k_layer1PKiS0_PKfPK6__halfS2_S2_P7__half2.kd
    .uniform_work_group_size: 1
    .uses_dynamic_stack: false
    .vgpr_count:     70
    .vgpr_spill_count: 0
    .wavefront_size: 64
  - .agpr_count:     0
    .args:
      - .actual_access:  read_only
        .address_space:  global
        .offset:         0
        .size:           8
        .value_kind:     global_buffer
      - .actual_access:  read_only
        .address_space:  global
        .offset:         8
        .size:           8
        .value_kind:     global_buffer
      - .actual_access:  read_only
        .address_space:  global
        .offset:         16
        .size:           8
        .value_kind:     global_buffer
      - .actual_access:  read_only
        .address_space:  global
        .offset:         24
        .size:           8
        .value_kind:     global_buffer
      - .actual_access:  read_only
        .address_space:  global
        .offset:         32
        .size:           8
        .value_kind:     global_buffer
      - .actual_access:  write_only
        .address_space:  global
        .offset:         40
        .size:           8
        .value_kind:     global_buffer
    .group_segment_fixed_size: 157408
    .kernarg_segment_align: 8
    .kernarg_segment_size: 48
    .language:       OpenCL C
    .language_version:
      - 2
      - 0
    .max_flat_workgroup_size: 1024
    .name:           _Z8k_layer2PKiS0_PKfPKjS2_P15HIP_vector_typeIfLj2EE
    .private_segment_fixed_size: 0
    .sgpr_count:     30
    .sgpr_spill_count: 0
    .symbol:         _Z8k_layer2PKiS0_PKfPKjS2_P15HIP_vector_typeIfLj2EE.kd
    .uniform_work_group_size: 1
    .uses_dynamic_stack: false
    .vgpr_count:     115
    .vgpr_spill_count: 0
    .wavefront_size: 64
  - .agpr_count:     0
    .args:
      - .actual_access:  read_only
        .address_space:  global
        .offset:         0
        .size:           8
        .value_kind:     global_buffer
      - .actual_access:  read_only
        .address_space:  global
        .offset:         8
        .size:           8
        .value_kind:     global_buffer
      - .actual_access:  write_only
        .address_space:  global
        .offset:         16
        .size:           8
        .value_kind:     global_buffer
    .group_segment_fixed_size: 0
    .kernarg_segment_align: 8
    .kernarg_segment_size: 24
    .language:       OpenCL C
    .language_version:
      - 2
      - 0
    .max_flat_workgroup_size: 256
    .name:           _Z5k_outPK15HIP_vector_typeIiLj4EEPKS_IfLj2EEPS3_
    .private_segment_fixed_size: 0
    .sgpr_count:     14
    .sgpr_spill_count: 0
    .symbol:         _Z5k_outPK15HIP_vector_typeIiLj4EEPKS_IfLj2EEPS3_.kd
    .uniform_work_group_size: 1
    .uses_dynamic_stack: false
    .vgpr_count:     14
    .vgpr_spill_count: 0
    .wavefront_size: 64
